# P7 merge epilogue: row-scale loads first, sigmoid run overlaps the projection loads (wait moved behind it)
# speedup vs baseline: 1.0027x; 1.0027x over previous
.LBB0_1047:
	s_lshl_b32 s4, s64, 8
	v_mov_b32_e32 v148, v0
	s_add_i32 s4, s4, s58
	s_mov_b32 s12, 0x20000
	v_and_or_b32 v212, v148, 15, s4
	s_lshl_b32 s4, s63, 6
	s_or_b32 s4, s4, s61
	v_lshrrev_b32_e32 v2, 2, v148
	v_and_or_b32 v214, v2, 12, s4
	v_ashrrev_i32_e32 v213, 31, v212
	v_lshl_add_u64 v[246:247], v[212:213], 2, s[20:21]
	global_load_dword v232, v[246:247], off
	global_load_dword v231, v[246:247], off offset:64
	global_load_dword v230, v[246:247], off offset:128
	global_load_dword v229, v[246:247], off offset:192
	global_load_dword v228, v[246:247], off offset:512
	global_load_dword v227, v[246:247], off offset:576
	global_load_dword v226, v[246:247], off offset:640
	global_load_dword v225, v[246:247], off offset:704
	v_ashrrev_i32_e32 v140, 3, v214
	v_lshlrev_b64 v[144:145], 3, v[212:213]
	v_ashrrev_i32_e32 v141, 31, v140
	v_and_b32_e32 v147, 0x3fffff, v145
	v_and_b32_e32 v146, 0xfffffe00, v144
	v_lshl_add_u64 v[146:147], v[146:147], 0, v[140:141]
	v_lshlrev_b64 v[146:147], 10, v[146:147]
	v_lshlrev_b32_e32 v2, 1, v144
	v_lshl_add_u64 v[146:147], s[18:19], 0, v[146:147]
	v_and_b32_e32 v2, 0xf0, v2
	v_lshl_add_u64 v[144:145], v[146:147], 0, v[2:3]
	v_lshrrev_b32_e32 v2, 1, v148
	v_or_b32_e32 v194, 16, v212
	v_and_b32_e32 v2, 8, v2
	v_ashrrev_i32_e32 v195, 31, v194
	v_lshl_add_u64 v[144:145], v[144:145], 0, v[2:3]
	v_lshlrev_b64 v[154:155], 3, v[194:195]
	v_add_co_u32_e32 v146, vcc, s12, v144
	v_and_b32_e32 v157, 0x3fffff, v155
	v_and_b32_e32 v156, 0xfffffe00, v154
	v_addc_co_u32_e32 v147, vcc, 0, v145, vcc
	s_mov_b32 s5, 0x40000
	v_lshl_add_u64 v[156:157], v[156:157], 0, v[140:141]
	v_add_co_u32_e32 v148, vcc, s5, v144
	v_lshlrev_b64 v[156:157], 10, v[156:157]
	v_lshlrev_b32_e32 v154, 1, v154
	v_addc_co_u32_e32 v149, vcc, 0, v145, vcc
	s_mov_b32 s4, 0x60000
	v_lshl_add_u64 v[156:157], s[18:19], 0, v[156:157]
	v_and_b32_e32 v154, 0x3f0, v154
	v_mov_b32_e32 v155, v3
	v_add_co_u32_e32 v150, vcc, s4, v144
	v_lshl_add_u64 v[154:155], v[156:157], 0, v[154:155]
	s_nop 0
	v_addc_co_u32_e32 v151, vcc, 0, v145, vcc
	v_lshl_add_u64 v[154:155], v[154:155], 0, v[2:3]
	v_lshl_add_u64 v[152:153], v[194:195], 2, s[20:21]
	global_load_dwordx2 v[218:219], v[148:149], off
	global_load_dwordx2 v[216:217], v[150:151], off
	global_load_dwordx2 v[204:205], v[154:155], off
	v_add_co_u32_e32 v148, vcc, s12, v154
	v_or_b32_e32 v184, 32, v212
	s_nop 0
	v_addc_co_u32_e32 v149, vcc, 0, v155, vcc
	v_add_co_u32_e32 v150, vcc, s5, v154
	v_ashrrev_i32_e32 v185, 31, v184
	s_nop 0
	v_addc_co_u32_e32 v151, vcc, 0, v155, vcc
	v_add_co_u32_e32 v152, vcc, s4, v154
	v_or_b32_e32 v174, 48, v212
	s_nop 0
	v_addc_co_u32_e32 v153, vcc, 0, v155, vcc
	v_lshl_add_u64 v[154:155], v[184:185], 2, s[20:21]
	global_load_dwordx2 v[210:211], v[148:149], off
	global_load_dwordx2 v[208:209], v[150:151], off
	global_load_dwordx2 v[206:207], v[152:153], off
	v_lshlrev_b64 v[148:149], 3, v[184:185]
	v_and_b32_e32 v151, 0x3fffff, v149
	v_and_b32_e32 v150, 0xfffffe00, v148
	v_lshl_add_u64 v[150:151], v[150:151], 0, v[140:141]
	v_lshlrev_b64 v[150:151], 10, v[150:151]
	v_lshlrev_b32_e32 v148, 1, v148
	v_lshl_add_u64 v[150:151], s[18:19], 0, v[150:151]
	v_and_b32_e32 v148, 0x3f0, v148
	v_mov_b32_e32 v149, v3
	v_lshl_add_u64 v[148:149], v[150:151], 0, v[148:149]
	v_lshl_add_u64 v[148:149], v[148:149], 0, v[2:3]
	v_add_co_u32_e32 v150, vcc, s12, v148
	v_ashrrev_i32_e32 v175, 31, v174
	s_nop 0
	v_addc_co_u32_e32 v151, vcc, 0, v149, vcc
	v_add_co_u32_e32 v152, vcc, s5, v148
	v_lshl_add_u64 v[142:143], v[212:213], 2, s[20:21]
	s_nop 0
	v_addc_co_u32_e32 v153, vcc, 0, v149, vcc
	v_add_co_u32_e32 v154, vcc, s4, v148
	v_add_u32_e32 v164, 0x80, v212
	s_nop 0
	v_addc_co_u32_e32 v155, vcc, 0, v149, vcc
	global_load_dwordx2 v[192:193], v[148:149], off
	global_load_dwordx2 v[190:191], v[150:151], off
	global_load_dwordx2 v[188:189], v[152:153], off
	global_load_dwordx2 v[186:187], v[154:155], off
	v_lshlrev_b64 v[150:151], 3, v[174:175]
	v_and_b32_e32 v153, 0x3fffff, v151
	v_and_b32_e32 v152, 0xfffffe00, v150
	v_lshl_add_u64 v[152:153], v[152:153], 0, v[140:141]
	v_lshlrev_b64 v[152:153], 10, v[152:153]
	v_lshlrev_b32_e32 v150, 1, v150
	v_lshl_add_u64 v[152:153], s[18:19], 0, v[152:153]
	v_and_b32_e32 v150, 0x3f0, v150
	v_mov_b32_e32 v151, v3
	v_lshl_add_u64 v[150:151], v[152:153], 0, v[150:151]
	v_lshl_add_u64 v[150:151], v[150:151], 0, v[2:3]
	v_add_co_u32_e32 v152, vcc, s12, v150
	v_lshl_add_u64 v[148:149], v[174:175], 2, s[20:21]
	s_nop 0
	v_addc_co_u32_e32 v153, vcc, 0, v151, vcc
	v_add_co_u32_e32 v154, vcc, s5, v150
	v_ashrrev_i32_e32 v165, 31, v164
	s_nop 0
	v_addc_co_u32_e32 v155, vcc, 0, v151, vcc
	global_load_dwordx2 v[180:181], v[150:151], off
	global_load_dwordx2 v[178:179], v[152:153], off
	global_load_dwordx2 v[176:177], v[154:155], off
	global_load_dwordx2 v[222:223], v[144:145], off
	global_load_dwordx2 v[220:221], v[146:147], off
	v_lshlrev_b64 v[142:143], 3, v[164:165]
	v_and_b32_e32 v145, 0x3fffff, v143
	v_and_b32_e32 v144, 0xfffffe00, v142
	v_lshl_add_u64 v[144:145], v[144:145], 0, v[140:141]
	v_lshlrev_b64 v[144:145], 10, v[144:145]
	v_lshlrev_b32_e32 v142, 1, v142
	v_lshl_add_u64 v[144:145], s[18:19], 0, v[144:145]
	v_and_b32_e32 v142, 0x3f0, v142
	v_mov_b32_e32 v143, v3
	v_add_co_u32_e32 v148, vcc, s4, v150
	v_lshl_add_u64 v[142:143], v[144:145], 0, v[142:143]
	s_nop 0
	v_addc_co_u32_e32 v149, vcc, 0, v151, vcc
	v_lshl_add_u64 v[142:143], v[142:143], 0, v[2:3]
	v_add_co_u32_e32 v144, vcc, s12, v142
	v_add_u32_e32 v196, 0xb0, v212
	s_nop 0
	v_addc_co_u32_e32 v145, vcc, 0, v143, vcc
	v_add_co_u32_e32 v146, vcc, s5, v142
	v_ashrrev_i32_e32 v197, 31, v196
	s_nop 0
	v_addc_co_u32_e32 v147, vcc, 0, v143, vcc
	global_load_dwordx2 v[182:183], v[148:149], off
	global_load_dwordx2 v[170:171], v[142:143], off
	global_load_dwordx2 v[168:169], v[144:145], off
	global_load_dwordx2 v[166:167], v[146:147], off
	v_add_u32_e32 v144, 0x90, v212
	v_ashrrev_i32_e32 v145, 31, v144
	v_lshl_add_u64 v[146:147], v[144:145], 2, s[20:21]
	v_lshlrev_b64 v[144:145], 3, v[144:145]
	v_and_b32_e32 v149, 0x3fffff, v145
	v_and_b32_e32 v148, 0xfffffe00, v144
	v_lshl_add_u64 v[148:149], v[148:149], 0, v[140:141]
	v_lshlrev_b64 v[148:149], 10, v[148:149]
	v_lshlrev_b32_e32 v144, 1, v144
	v_lshl_add_u64 v[148:149], s[18:19], 0, v[148:149]
	v_and_b32_e32 v144, 0x3f0, v144
	v_mov_b32_e32 v145, v3
	v_add_co_u32_e32 v142, vcc, s4, v142
	v_lshl_add_u64 v[144:145], v[148:149], 0, v[144:145]
	s_nop 0
	v_addc_co_u32_e32 v143, vcc, 0, v143, vcc
	v_lshl_add_u64 v[144:145], v[144:145], 0, v[2:3]
	v_add_co_u32_e32 v148, vcc, s12, v144
	v_lshl_add_u64 v[198:199], v[196:197], 2, s[20:21]
	s_nop 0
	v_addc_co_u32_e32 v149, vcc, 0, v145, vcc
	global_load_dwordx2 v[172:173], v[142:143], off
	global_load_dwordx2 v[158:159], v[144:145], off
	global_load_dwordx2 v[156:157], v[148:149], off
	v_add_u32_e32 v146, 0xa0, v212
	v_ashrrev_i32_e32 v147, 31, v146
	v_lshl_add_u64 v[148:149], v[146:147], 2, s[20:21]
	v_lshlrev_b64 v[146:147], 3, v[146:147]
	v_and_b32_e32 v151, 0x3fffff, v147
	v_and_b32_e32 v150, 0xfffffe00, v146
	v_lshl_add_u64 v[150:151], v[150:151], 0, v[140:141]
	v_add_co_u32_e32 v142, vcc, s5, v144
	v_lshlrev_b64 v[150:151], 10, v[150:151]
	v_lshlrev_b32_e32 v146, 1, v146
	v_addc_co_u32_e32 v143, vcc, 0, v145, vcc
	v_lshl_add_u64 v[150:151], s[18:19], 0, v[150:151]
	v_and_b32_e32 v146, 0x3f0, v146
	v_mov_b32_e32 v147, v3
	v_add_co_u32_e32 v144, vcc, s4, v144
	v_lshl_add_u64 v[146:147], v[150:151], 0, v[146:147]
	s_nop 0
	v_addc_co_u32_e32 v145, vcc, 0, v145, vcc
	v_lshl_add_u64 v[146:147], v[146:147], 0, v[2:3]
	global_load_dwordx2 v[162:163], v[142:143], off
	global_load_dwordx2 v[160:161], v[144:145], off
	s_nop 0
	global_load_dwordx2 v[148:149], v[146:147], off
	v_add_co_u32_e32 v142, vcc, s12, v146
	s_waitcnt vmcnt(25)
	v_mul_f32_e64 v108, v231, -v108
	v_addc_co_u32_e32 v143, vcc, 0, v147, vcc
	v_add_co_u32_e32 v144, vcc, s5, v146
	v_mul_f32_e64 v124, v232, -v124
	s_nop 0
	v_addc_co_u32_e32 v145, vcc, 0, v147, vcc
	v_add_co_u32_e32 v146, vcc, s4, v146
	v_mul_f32_e32 v124, 0x3fb8aa3b, v124
	s_nop 0
	v_addc_co_u32_e32 v147, vcc, 0, v147, vcc
	global_load_dwordx2 v[154:155], v[142:143], off
	global_load_dwordx2 v[152:153], v[144:145], off
	global_load_dwordx2 v[150:151], v[146:147], off
	v_lshlrev_b64 v[142:143], 3, v[196:197]
	v_and_b32_e32 v145, 0x3fffff, v143
	v_and_b32_e32 v144, 0xfffffe00, v142
	v_lshl_add_u64 v[140:141], v[144:145], 0, v[140:141]
	v_lshlrev_b64 v[140:141], 10, v[140:141]
	v_lshlrev_b32_e32 v142, 1, v142
	v_lshl_add_u64 v[140:141], s[18:19], 0, v[140:141]
	v_and_b32_e32 v142, 0x3f0, v142
	v_mov_b32_e32 v143, v3
	v_lshl_add_u64 v[140:141], v[140:141], 0, v[142:143]
	v_lshl_add_u64 v[140:141], v[140:141], 0, v[2:3]
	v_mul_f32_e64 v2, v232, -v128
	v_mul_f32_e32 v2, 0x3fb8aa3b, v2
	v_mul_f32_e64 v128, v232, -v129
	v_exp_f32_e32 v2, v2
	v_mul_f32_e32 v128, 0x3fb8aa3b, v128
	v_exp_f32_e32 v129, v128
	v_mul_f32_e64 v125, v232, -v125
	v_add_f32_e32 v2, 1.0, v2
	v_rcp_f32_e32 v128, v2
	v_add_f32_e32 v2, 1.0, v129
	v_mul_f32_e64 v129, v232, -v130
	v_mul_f32_e32 v129, 0x3fb8aa3b, v129
	v_exp_f32_e32 v130, v129
	v_mul_f32_e64 v129, v232, -v131
	v_mul_f32_e32 v129, 0x3fb8aa3b, v129
	v_exp_f32_e32 v131, v129
	v_exp_f32_e32 v124, v124
	v_mul_f32_e32 v125, 0x3fb8aa3b, v125
	v_exp_f32_e32 v125, v125
	v_rcp_f32_e32 v129, v2
	v_add_f32_e32 v2, 1.0, v130
	v_rcp_f32_e32 v130, v2
	v_add_f32_e32 v2, 1.0, v131
	v_rcp_f32_e32 v131, v2
	v_add_f32_e32 v2, 1.0, v124
	v_rcp_f32_e32 v124, v2
	v_add_f32_e32 v2, 1.0, v125
	v_mul_f32_e64 v125, v232, -v126
	v_mul_f32_e32 v125, 0x3fb8aa3b, v125
	v_exp_f32_e32 v126, v125
	v_mul_f32_e64 v125, v232, -v127
	v_mul_f32_e32 v125, 0x3fb8aa3b, v125
	v_mul_f32_e64 v120, v232, -v120
	v_exp_f32_e32 v127, v125
	v_mul_f32_e32 v120, 0x3fb8aa3b, v120
	v_mul_f32_e64 v121, v232, -v121
	v_exp_f32_e32 v120, v120
	v_mul_f32_e32 v121, 0x3fb8aa3b, v121
	v_exp_f32_e32 v121, v121
	v_rcp_f32_e32 v125, v2
	v_add_f32_e32 v2, 1.0, v126
	v_rcp_f32_e32 v126, v2
	v_add_f32_e32 v2, 1.0, v127
	v_rcp_f32_e32 v127, v2
	v_add_f32_e32 v2, 1.0, v120
	v_rcp_f32_e32 v120, v2
	v_add_f32_e32 v2, 1.0, v121
	v_mul_f32_e64 v121, v232, -v122
	v_mul_f32_e32 v121, 0x3fb8aa3b, v121
	v_exp_f32_e32 v122, v121
	v_mul_f32_e64 v121, v232, -v123
	v_mul_f32_e32 v121, 0x3fb8aa3b, v121
	v_mul_f32_e64 v116, v232, -v116
	v_exp_f32_e32 v123, v121
	v_mul_f32_e32 v116, 0x3fb8aa3b, v116
	v_mul_f32_e64 v117, v232, -v117
	v_exp_f32_e32 v116, v116
	v_mul_f32_e32 v117, 0x3fb8aa3b, v117
	v_exp_f32_e32 v117, v117
	v_rcp_f32_e32 v121, v2
	v_add_f32_e32 v2, 1.0, v122
	v_rcp_f32_e32 v122, v2
	v_add_f32_e32 v2, 1.0, v123
	v_rcp_f32_e32 v123, v2
	v_add_f32_e32 v2, 1.0, v116
	v_rcp_f32_e32 v116, v2
	v_add_f32_e32 v2, 1.0, v117
	v_rcp_f32_e32 v117, v2
	v_mul_f32_e64 v2, v232, -v118
	v_mul_f32_e32 v2, 0x3fb8aa3b, v2
	v_mul_f32_e64 v118, v232, -v119
	v_exp_f32_e32 v2, v2
	v_mul_f32_e32 v118, 0x3fb8aa3b, v118
	v_exp_f32_e32 v119, v118
	v_mul_f32_e32 v108, 0x3fb8aa3b, v108
	v_add_f32_e32 v2, 1.0, v2
	v_rcp_f32_e32 v118, v2
	v_add_f32_e32 v2, 1.0, v119
	v_rcp_f32_e32 v119, v2
	v_mul_f32_e64 v2, v231, -v112
	v_mul_f32_e32 v2, 0x3fb8aa3b, v2
	v_mul_f32_e64 v112, v231, -v113
	v_exp_f32_e32 v2, v2
	v_mul_f32_e32 v112, 0x3fb8aa3b, v112
	v_exp_f32_e32 v113, v112
	v_mul_f32_e64 v109, v231, -v109
	v_add_f32_e32 v2, 1.0, v2
	v_rcp_f32_e32 v112, v2
	v_add_f32_e32 v2, 1.0, v113
	v_mul_f32_e64 v113, v231, -v114
	v_mul_f32_e32 v113, 0x3fb8aa3b, v113
	v_exp_f32_e32 v114, v113
	v_mul_f32_e64 v113, v231, -v115
	v_mul_f32_e32 v113, 0x3fb8aa3b, v113
	v_exp_f32_e32 v115, v113
	v_exp_f32_e32 v108, v108
	v_mul_f32_e32 v109, 0x3fb8aa3b, v109
	v_exp_f32_e32 v109, v109
	v_rcp_f32_e32 v113, v2
	v_add_f32_e32 v2, 1.0, v114
	v_rcp_f32_e32 v114, v2
	v_add_f32_e32 v2, 1.0, v115
	v_rcp_f32_e32 v115, v2
	v_add_f32_e32 v2, 1.0, v108
	v_rcp_f32_e32 v108, v2
	v_add_f32_e32 v2, 1.0, v109
	v_mul_f32_e64 v109, v231, -v110
	v_mul_f32_e32 v109, 0x3fb8aa3b, v109
	v_exp_f32_e32 v110, v109
	v_mul_f32_e64 v109, v231, -v111
	v_mul_f32_e32 v109, 0x3fb8aa3b, v109
	v_mul_f32_e64 v104, v231, -v104
	v_exp_f32_e32 v111, v109
	v_mul_f32_e32 v104, 0x3fb8aa3b, v104
	v_mul_f32_e64 v105, v231, -v105
	v_exp_f32_e32 v104, v104
	v_mul_f32_e32 v105, 0x3fb8aa3b, v105
	v_exp_f32_e32 v105, v105
	v_rcp_f32_e32 v109, v2
	v_add_f32_e32 v2, 1.0, v110
	v_rcp_f32_e32 v110, v2
	v_add_f32_e32 v2, 1.0, v111
	v_rcp_f32_e32 v111, v2
	v_add_f32_e32 v2, 1.0, v104
	v_rcp_f32_e32 v104, v2
	v_add_f32_e32 v2, 1.0, v105
	v_mul_f32_e64 v105, v231, -v106
	v_mul_f32_e32 v105, 0x3fb8aa3b, v105
	v_exp_f32_e32 v106, v105
	v_mul_f32_e64 v105, v231, -v107
	v_mul_f32_e32 v105, 0x3fb8aa3b, v105
	v_mul_f32_e64 v100, v231, -v100
	v_exp_f32_e32 v107, v105
	v_mul_f32_e32 v100, 0x3fb8aa3b, v100
	v_mul_f32_e64 v101, v231, -v101
	v_exp_f32_e32 v100, v100
	v_mul_f32_e32 v101, 0x3fb8aa3b, v101
	v_exp_f32_e32 v101, v101
	v_rcp_f32_e32 v105, v2
	v_add_f32_e32 v2, 1.0, v106
	v_rcp_f32_e32 v106, v2
	v_add_f32_e32 v2, 1.0, v107
	v_rcp_f32_e32 v107, v2
	v_add_f32_e32 v2, 1.0, v100
	v_rcp_f32_e32 v100, v2
	v_add_f32_e32 v2, 1.0, v101
	v_rcp_f32_e32 v101, v2
	v_mul_f32_e64 v2, v231, -v102
	v_mul_f32_e32 v2, 0x3fb8aa3b, v2
	v_mul_f32_e64 v102, v231, -v103
	v_exp_f32_e32 v2, v2
	v_mul_f32_e32 v102, 0x3fb8aa3b, v102
	v_exp_f32_e32 v103, v102
	v_mul_f32_e64 v92, v230, -v92
	v_add_f32_e32 v2, 1.0, v2
	v_rcp_f32_e32 v102, v2
	v_add_f32_e32 v2, 1.0, v103
	v_rcp_f32_e32 v103, v2
	v_mul_f32_e64 v2, v230, -v96
	v_mul_f32_e32 v2, 0x3fb8aa3b, v2
	v_mul_f32_e64 v96, v230, -v97
	v_exp_f32_e32 v2, v2
	v_mul_f32_e32 v96, 0x3fb8aa3b, v96
	v_exp_f32_e32 v97, v96
	v_mul_f32_e32 v92, 0x3fb8aa3b, v92
	v_add_f32_e32 v2, 1.0, v2
	v_rcp_f32_e32 v96, v2
	v_add_f32_e32 v2, 1.0, v97
	v_mul_f32_e64 v97, v230, -v98
	v_mul_f32_e32 v97, 0x3fb8aa3b, v97
	v_exp_f32_e32 v98, v97
	v_mul_f32_e64 v97, v230, -v99
	v_mul_f32_e32 v97, 0x3fb8aa3b, v97
	v_exp_f32_e32 v99, v97
	v_mul_f32_e64 v93, v230, -v93
	v_exp_f32_e32 v92, v92
	v_mul_f32_e32 v93, 0x3fb8aa3b, v93
	v_exp_f32_e32 v93, v93
	v_rcp_f32_e32 v97, v2
	v_add_f32_e32 v2, 1.0, v98
	v_rcp_f32_e32 v98, v2
	v_add_f32_e32 v2, 1.0, v99
	v_rcp_f32_e32 v99, v2
	v_add_f32_e32 v2, 1.0, v92
	v_rcp_f32_e32 v92, v2
	v_add_f32_e32 v2, 1.0, v93
	v_mul_f32_e64 v93, v230, -v94
	v_mul_f32_e32 v93, 0x3fb8aa3b, v93
	v_exp_f32_e32 v94, v93
	v_mul_f32_e64 v93, v230, -v95
	v_mul_f32_e32 v93, 0x3fb8aa3b, v93
	v_mul_f32_e64 v88, v230, -v88
	v_exp_f32_e32 v95, v93
	v_mul_f32_e32 v88, 0x3fb8aa3b, v88
	v_mul_f32_e64 v89, v230, -v89
	v_exp_f32_e32 v88, v88
	v_mul_f32_e32 v89, 0x3fb8aa3b, v89
	v_exp_f32_e32 v89, v89
	v_rcp_f32_e32 v93, v2
	v_add_f32_e32 v2, 1.0, v94
	v_rcp_f32_e32 v94, v2
	v_add_f32_e32 v2, 1.0, v95
	v_rcp_f32_e32 v95, v2
	v_add_f32_e32 v2, 1.0, v88
	v_rcp_f32_e32 v88, v2
	v_add_f32_e32 v2, 1.0, v89
	v_mul_f32_e64 v89, v230, -v90
	v_mul_f32_e32 v89, 0x3fb8aa3b, v89
	v_exp_f32_e32 v90, v89
	v_mul_f32_e64 v89, v230, -v91
	v_mul_f32_e32 v89, 0x3fb8aa3b, v89
	v_mul_f32_e64 v84, v230, -v84
	v_exp_f32_e32 v91, v89
	v_mul_f32_e32 v84, 0x3fb8aa3b, v84
	v_mul_f32_e64 v85, v230, -v85
	v_exp_f32_e32 v84, v84
	v_mul_f32_e32 v85, 0x3fb8aa3b, v85
	v_exp_f32_e32 v85, v85
	v_rcp_f32_e32 v89, v2
	v_add_f32_e32 v2, 1.0, v90
	v_rcp_f32_e32 v90, v2
	v_add_f32_e32 v2, 1.0, v91
	v_rcp_f32_e32 v91, v2
	v_add_f32_e32 v2, 1.0, v84
	v_rcp_f32_e32 v84, v2
	v_add_f32_e32 v2, 1.0, v85
	v_rcp_f32_e32 v85, v2
	v_mul_f32_e64 v2, v230, -v86
	v_mul_f32_e32 v2, 0x3fb8aa3b, v2
	v_mul_f32_e64 v86, v230, -v87
	v_exp_f32_e32 v2, v2
	v_mul_f32_e32 v86, 0x3fb8aa3b, v86
	v_exp_f32_e32 v87, v86
	v_mul_f32_e64 v76, v229, -v76
	v_add_f32_e32 v2, 1.0, v2
	v_rcp_f32_e32 v86, v2
	v_add_f32_e32 v2, 1.0, v87
	v_rcp_f32_e32 v87, v2
	v_mul_f32_e64 v2, v229, -v80
	v_mul_f32_e32 v2, 0x3fb8aa3b, v2
	v_mul_f32_e64 v80, v229, -v81
	v_exp_f32_e32 v2, v2
	v_mul_f32_e32 v80, 0x3fb8aa3b, v80
	v_exp_f32_e32 v81, v80
	v_mul_f32_e32 v76, 0x3fb8aa3b, v76
	v_add_f32_e32 v2, 1.0, v2
	v_rcp_f32_e32 v80, v2
	v_add_f32_e32 v2, 1.0, v81
	v_mul_f32_e64 v81, v229, -v82
	v_mul_f32_e32 v81, 0x3fb8aa3b, v81
	v_exp_f32_e32 v82, v81
	v_mul_f32_e64 v81, v229, -v83
	v_mul_f32_e32 v81, 0x3fb8aa3b, v81
	v_exp_f32_e32 v83, v81
	v_mul_f32_e64 v77, v229, -v77
	v_exp_f32_e32 v76, v76
	v_mul_f32_e32 v77, 0x3fb8aa3b, v77
	v_exp_f32_e32 v77, v77
	v_rcp_f32_e32 v81, v2
	v_add_f32_e32 v2, 1.0, v82
	v_rcp_f32_e32 v82, v2
	v_add_f32_e32 v2, 1.0, v83
	v_rcp_f32_e32 v83, v2
	v_add_f32_e32 v2, 1.0, v76
	v_rcp_f32_e32 v76, v2
	v_add_f32_e32 v2, 1.0, v77
	v_mul_f32_e64 v77, v229, -v78
	v_mul_f32_e32 v77, 0x3fb8aa3b, v77
	v_exp_f32_e32 v78, v77
	v_mul_f32_e64 v77, v229, -v79
	v_mul_f32_e32 v77, 0x3fb8aa3b, v77
	v_mul_f32_e64 v72, v229, -v72
	v_exp_f32_e32 v79, v77
	v_mul_f32_e32 v72, 0x3fb8aa3b, v72
	v_mul_f32_e64 v73, v229, -v73
	v_exp_f32_e32 v72, v72
	v_mul_f32_e32 v73, 0x3fb8aa3b, v73
	v_exp_f32_e32 v73, v73
	v_rcp_f32_e32 v77, v2
	v_add_f32_e32 v2, 1.0, v78
	v_rcp_f32_e32 v78, v2
	v_add_f32_e32 v2, 1.0, v79
	v_rcp_f32_e32 v79, v2
	v_add_f32_e32 v2, 1.0, v72
	v_rcp_f32_e32 v72, v2
	v_add_f32_e32 v2, 1.0, v73
	v_mul_f32_e64 v73, v229, -v74
	v_mul_f32_e32 v73, 0x3fb8aa3b, v73
	v_exp_f32_e32 v74, v73
	v_mul_f32_e64 v73, v229, -v75
	v_mul_f32_e32 v73, 0x3fb8aa3b, v73
	v_mul_f32_e64 v68, v229, -v68
	v_exp_f32_e32 v75, v73
	v_mul_f32_e32 v68, 0x3fb8aa3b, v68
	v_mul_f32_e64 v69, v229, -v69
	v_exp_f32_e32 v68, v68
	v_mul_f32_e32 v69, 0x3fb8aa3b, v69
	v_exp_f32_e32 v69, v69
	v_rcp_f32_e32 v73, v2
	v_add_f32_e32 v2, 1.0, v74
	v_rcp_f32_e32 v74, v2
	v_add_f32_e32 v2, 1.0, v75
	v_rcp_f32_e32 v75, v2
	v_add_f32_e32 v2, 1.0, v68
	v_rcp_f32_e32 v68, v2
	v_add_f32_e32 v2, 1.0, v69
	v_rcp_f32_e32 v69, v2
	v_mul_f32_e64 v2, v229, -v70
	v_mul_f32_e32 v2, 0x3fb8aa3b, v2
	v_mul_f32_e64 v70, v229, -v71
	v_exp_f32_e32 v2, v2
	v_mul_f32_e32 v70, 0x3fb8aa3b, v70
	v_exp_f32_e32 v71, v70
	v_mul_f32_e64 v60, v228, -v60
	v_add_f32_e32 v2, 1.0, v2
	v_rcp_f32_e32 v70, v2
	v_add_f32_e32 v2, 1.0, v71
	v_rcp_f32_e32 v71, v2
	v_mul_f32_e64 v2, v228, -v64
	v_mul_f32_e32 v2, 0x3fb8aa3b, v2
	v_mul_f32_e64 v64, v228, -v65
	v_exp_f32_e32 v2, v2
	v_mul_f32_e32 v64, 0x3fb8aa3b, v64
	v_exp_f32_e32 v65, v64
	v_mul_f32_e32 v60, 0x3fb8aa3b, v60
	v_add_f32_e32 v2, 1.0, v2
	v_rcp_f32_e32 v64, v2
	v_add_f32_e32 v2, 1.0, v65
	v_mul_f32_e64 v65, v228, -v66
	v_mul_f32_e32 v65, 0x3fb8aa3b, v65
	v_exp_f32_e32 v66, v65
	v_mul_f32_e64 v65, v228, -v67
	v_mul_f32_e32 v65, 0x3fb8aa3b, v65
	v_exp_f32_e32 v67, v65
	v_mul_f32_e64 v61, v228, -v61
	v_exp_f32_e32 v60, v60
	v_mul_f32_e32 v61, 0x3fb8aa3b, v61
	v_exp_f32_e32 v61, v61
	v_rcp_f32_e32 v65, v2
	v_add_f32_e32 v2, 1.0, v66
	v_rcp_f32_e32 v66, v2
	v_add_f32_e32 v2, 1.0, v67
	v_rcp_f32_e32 v67, v2
	v_add_f32_e32 v2, 1.0, v60
	v_rcp_f32_e32 v60, v2
	v_add_f32_e32 v2, 1.0, v61
	v_mul_f32_e64 v61, v228, -v62
	v_mul_f32_e32 v61, 0x3fb8aa3b, v61
	v_exp_f32_e32 v62, v61
	v_mul_f32_e64 v61, v228, -v63
	v_mul_f32_e32 v61, 0x3fb8aa3b, v61
	v_mul_f32_e64 v56, v228, -v56
	v_exp_f32_e32 v63, v61
	v_mul_f32_e32 v56, 0x3fb8aa3b, v56
	v_mul_f32_e64 v57, v228, -v57
	v_exp_f32_e32 v56, v56
	v_mul_f32_e32 v57, 0x3fb8aa3b, v57
	v_exp_f32_e32 v57, v57
	v_rcp_f32_e32 v61, v2
	v_add_f32_e32 v2, 1.0, v62
	v_rcp_f32_e32 v62, v2
	v_add_f32_e32 v2, 1.0, v63
	v_rcp_f32_e32 v63, v2
	v_add_f32_e32 v2, 1.0, v56
	v_rcp_f32_e32 v56, v2
	v_add_f32_e32 v2, 1.0, v57
	v_mul_f32_e64 v57, v228, -v58
	v_mul_f32_e32 v57, 0x3fb8aa3b, v57
	v_exp_f32_e32 v58, v57
	v_mul_f32_e64 v57, v228, -v59
	v_mul_f32_e32 v57, 0x3fb8aa3b, v57
	v_mul_f32_e64 v52, v228, -v52
	v_exp_f32_e32 v59, v57
	v_mul_f32_e32 v52, 0x3fb8aa3b, v52
	v_mul_f32_e64 v53, v228, -v53
	v_exp_f32_e32 v52, v52
	v_mul_f32_e32 v53, 0x3fb8aa3b, v53
	v_exp_f32_e32 v53, v53
	v_rcp_f32_e32 v57, v2
	v_add_f32_e32 v2, 1.0, v58
	v_rcp_f32_e32 v58, v2
	v_add_f32_e32 v2, 1.0, v59
	v_rcp_f32_e32 v59, v2
	v_add_f32_e32 v2, 1.0, v52
	v_rcp_f32_e32 v52, v2
	v_add_f32_e32 v2, 1.0, v53
	v_rcp_f32_e32 v53, v2
	v_mul_f32_e64 v2, v228, -v54
	v_mul_f32_e32 v2, 0x3fb8aa3b, v2
	v_mul_f32_e64 v54, v228, -v55
	v_exp_f32_e32 v2, v2
	v_mul_f32_e32 v54, 0x3fb8aa3b, v54
	v_exp_f32_e32 v55, v54
	v_mul_f32_e64 v44, v227, -v44
	v_add_f32_e32 v2, 1.0, v2
	v_rcp_f32_e32 v54, v2
	v_add_f32_e32 v2, 1.0, v55
	v_rcp_f32_e32 v55, v2
	v_mul_f32_e64 v2, v227, -v48
	v_mul_f32_e32 v2, 0x3fb8aa3b, v2
	v_mul_f32_e64 v48, v227, -v49
	v_exp_f32_e32 v2, v2
	v_mul_f32_e32 v48, 0x3fb8aa3b, v48
	v_exp_f32_e32 v49, v48
	v_mul_f32_e32 v44, 0x3fb8aa3b, v44
	v_add_f32_e32 v2, 1.0, v2
	v_rcp_f32_e32 v48, v2
	v_add_f32_e32 v2, 1.0, v49
	v_mul_f32_e64 v49, v227, -v50
	v_mul_f32_e32 v49, 0x3fb8aa3b, v49
	v_exp_f32_e32 v50, v49
	v_mul_f32_e64 v49, v227, -v51
	v_mul_f32_e32 v49, 0x3fb8aa3b, v49
	v_exp_f32_e32 v51, v49
	v_mul_f32_e64 v45, v227, -v45
	v_exp_f32_e32 v44, v44
	v_mul_f32_e32 v45, 0x3fb8aa3b, v45
	v_exp_f32_e32 v45, v45
	v_rcp_f32_e32 v49, v2
	v_add_f32_e32 v2, 1.0, v50
	v_rcp_f32_e32 v50, v2
	v_add_f32_e32 v2, 1.0, v51
	v_rcp_f32_e32 v51, v2
	v_add_f32_e32 v2, 1.0, v44
	v_rcp_f32_e32 v44, v2
	v_add_f32_e32 v2, 1.0, v45
	v_mul_f32_e64 v45, v227, -v46
	v_mul_f32_e32 v45, 0x3fb8aa3b, v45
	v_exp_f32_e32 v46, v45
	v_mul_f32_e64 v45, v227, -v47
	v_mul_f32_e32 v45, 0x3fb8aa3b, v45
	v_mul_f32_e64 v40, v227, -v40
	v_exp_f32_e32 v47, v45
	v_mul_f32_e32 v40, 0x3fb8aa3b, v40
	v_mul_f32_e64 v41, v227, -v41
	v_exp_f32_e32 v40, v40
	v_mul_f32_e32 v41, 0x3fb8aa3b, v41
	v_exp_f32_e32 v41, v41
	v_rcp_f32_e32 v45, v2
	v_add_f32_e32 v2, 1.0, v46
	v_rcp_f32_e32 v46, v2
	v_add_f32_e32 v2, 1.0, v47
	v_rcp_f32_e32 v47, v2
	v_add_f32_e32 v2, 1.0, v40
	v_rcp_f32_e32 v40, v2
	v_add_f32_e32 v2, 1.0, v41
	v_mul_f32_e64 v41, v227, -v42
	v_mul_f32_e32 v41, 0x3fb8aa3b, v41
	v_exp_f32_e32 v42, v41
	v_mul_f32_e64 v41, v227, -v43
	v_mul_f32_e32 v41, 0x3fb8aa3b, v41
	v_mul_f32_e64 v36, v227, -v36
	v_exp_f32_e32 v43, v41
	v_mul_f32_e32 v36, 0x3fb8aa3b, v36
	v_mul_f32_e64 v37, v227, -v37
	v_exp_f32_e32 v36, v36
	v_mul_f32_e32 v37, 0x3fb8aa3b, v37
	v_exp_f32_e32 v37, v37
	v_rcp_f32_e32 v41, v2
	v_add_f32_e32 v2, 1.0, v42
	v_rcp_f32_e32 v42, v2
	v_add_f32_e32 v2, 1.0, v43
	v_rcp_f32_e32 v43, v2
	v_add_f32_e32 v2, 1.0, v36
	v_rcp_f32_e32 v36, v2
	v_add_f32_e32 v2, 1.0, v37
	v_rcp_f32_e32 v37, v2
	v_mul_f32_e64 v2, v227, -v38
	v_mul_f32_e32 v2, 0x3fb8aa3b, v2
	v_mul_f32_e64 v38, v227, -v39
	v_exp_f32_e32 v2, v2
	v_mul_f32_e32 v38, 0x3fb8aa3b, v38
	v_exp_f32_e32 v39, v38
	s_waitcnt vmcnt(0)
	v_add_co_u32_e32 v142, vcc, s12, v140
	v_add_f32_e32 v2, 1.0, v2
	v_rcp_f32_e32 v38, v2
	v_add_f32_e32 v2, 1.0, v39
	v_rcp_f32_e32 v39, v2
	v_mul_f32_e64 v2, v226, -v32
	v_mul_f32_e32 v2, 0x3fb8aa3b, v2
	v_mul_f32_e64 v32, v226, -v33
	v_exp_f32_e32 v2, v2
	v_mul_f32_e32 v32, 0x3fb8aa3b, v32
	v_addc_co_u32_e32 v143, vcc, 0, v141, vcc
	v_exp_f32_e32 v33, v32
	v_add_co_u32_e32 v196, vcc, s5, v140
	v_add_f32_e32 v2, 1.0, v2
	s_nop 0
	v_addc_co_u32_e32 v197, vcc, 0, v141, vcc
	v_add_co_u32_e32 v198, vcc, s4, v140
	v_rcp_f32_e32 v32, v2
	s_nop 0
	v_addc_co_u32_e32 v199, vcc, 0, v141, vcc
	global_load_dwordx2 v[146:147], v[140:141], off
	global_load_dwordx2 v[144:145], v[142:143], off
	s_nop 0
	global_load_dwordx2 v[142:143], v[196:197], off
	global_load_dwordx2 v[140:141], v[198:199], off
	v_lshlrev_b32_e32 v196, 16, v222
	v_and_b32_e32 v197, 0xffff0000, v222
	v_add_f32_e32 v2, 1.0, v33
	v_mul_f32_e64 v33, v226, -v34
	v_pk_fma_f32 v[128:129], v[128:129], v[196:197], 0 op_sel_hi:[1,1,0]
	v_lshlrev_b32_e32 v196, 16, v220
	v_and_b32_e32 v197, 0xffff0000, v220
	v_mul_f32_e32 v33, 0x3fb8aa3b, v33
	v_pk_fma_f32 v[124:125], v[124:125], v[196:197], v[128:129]
	v_lshlrev_b32_e32 v128, 16, v218
	v_and_b32_e32 v129, 0xffff0000, v218
	v_exp_f32_e32 v34, v33
	v_mul_f32_e64 v33, v226, -v35
	v_pk_fma_f32 v[120:121], v[120:121], v[128:129], v[124:125]
	v_lshlrev_b32_e32 v124, 16, v216
	v_and_b32_e32 v125, 0xffff0000, v216
	v_mul_f32_e32 v33, 0x3fb8aa3b, v33
	v_mul_f32_e64 v28, v226, -v28
	v_pk_fma_f32 v[116:117], v[116:117], v[124:125], v[120:121]
	v_lshlrev_b32_e32 v120, 16, v223
	v_and_b32_e32 v121, 0xffff0000, v223
	v_exp_f32_e32 v35, v33
	v_mul_f32_e32 v28, 0x3fb8aa3b, v28
	v_mul_f32_e64 v29, v226, -v29
	v_pk_fma_f32 v[120:121], v[130:131], v[120:121], 0 op_sel_hi:[1,1,0]
	v_lshlrev_b32_e32 v124, 16, v221
	v_and_b32_e32 v125, 0xffff0000, v221
	v_exp_f32_e32 v28, v28
	v_mul_f32_e32 v29, 0x3fb8aa3b, v29
	v_pk_fma_f32 v[120:121], v[126:127], v[124:125], v[120:121]
	v_lshlrev_b32_e32 v124, 16, v219
	v_and_b32_e32 v125, 0xffff0000, v219
	v_exp_f32_e32 v29, v29
	v_pk_fma_f32 v[120:121], v[122:123], v[124:125], v[120:121]
	v_lshlrev_b32_e32 v122, 16, v217
	v_and_b32_e32 v123, 0xffff0000, v217
	v_rcp_f32_e32 v33, v2
	v_add_f32_e32 v2, 1.0, v34
	v_ashrrev_i32_e32 v215, 31, v214
	v_pk_fma_f32 v[118:119], v[118:119], v[122:123], v[120:121]
	v_cvt_pk_bf16_f32 v120, v116, v117
	v_lshlrev_b64 v[116:117], 11, v[212:213]
	v_rcp_f32_e32 v34, v2
	v_add_f32_e32 v2, 1.0, v35
	v_cvt_pk_bf16_f32 v121, v118, v119
	v_lshl_add_u64 v[116:117], s[14:15], 0, v[116:117]
	v_lshlrev_b64 v[118:119], 1, v[214:215]
	v_rcp_f32_e32 v35, v2
	v_add_f32_e32 v2, 1.0, v28
	v_lshl_add_u64 v[116:117], v[116:117], 0, v[118:119]
	v_rcp_f32_e32 v28, v2
	v_add_f32_e32 v2, 1.0, v29
	v_mul_f32_e64 v29, v226, -v30
	global_store_dwordx2 v[116:117], v[120:121], off
	v_lshlrev_b32_e32 v120, 16, v204
	v_and_b32_e32 v121, 0xffff0000, v204
	v_mul_f32_e32 v29, 0x3fb8aa3b, v29
	v_pk_fma_f32 v[112:113], v[112:113], v[120:121], 0 op_sel_hi:[1,1,0]
	v_lshlrev_b32_e32 v120, 16, v210
	v_and_b32_e32 v121, 0xffff0000, v210
	v_exp_f32_e32 v30, v29
	v_mul_f32_e64 v29, v226, -v31
	v_pk_fma_f32 v[108:109], v[108:109], v[120:121], v[112:113]
	v_lshlrev_b32_e32 v112, 16, v208
	v_and_b32_e32 v113, 0xffff0000, v208
	v_mul_f32_e32 v29, 0x3fb8aa3b, v29
	v_mul_f32_e64 v24, v226, -v24
	v_pk_fma_f32 v[104:105], v[104:105], v[112:113], v[108:109]
	v_lshlrev_b32_e32 v108, 16, v206
	v_and_b32_e32 v109, 0xffff0000, v206
	v_exp_f32_e32 v31, v29
	v_mul_f32_e32 v24, 0x3fb8aa3b, v24
	v_mul_f32_e64 v25, v226, -v25
	v_pk_fma_f32 v[100:101], v[100:101], v[108:109], v[104:105]
	v_lshlrev_b32_e32 v104, 16, v205
	v_and_b32_e32 v105, 0xffff0000, v205
	v_exp_f32_e32 v24, v24
	v_mul_f32_e32 v25, 0x3fb8aa3b, v25
	v_pk_fma_f32 v[104:105], v[114:115], v[104:105], 0 op_sel_hi:[1,1,0]
	v_lshlrev_b32_e32 v108, 16, v211
	v_and_b32_e32 v109, 0xffff0000, v211
	v_exp_f32_e32 v25, v25
	v_pk_fma_f32 v[104:105], v[110:111], v[108:109], v[104:105]
	v_lshlrev_b32_e32 v108, 16, v209
	v_and_b32_e32 v109, 0xffff0000, v209
	v_rcp_f32_e32 v29, v2
	v_add_f32_e32 v2, 1.0, v30
	v_pk_fma_f32 v[104:105], v[106:107], v[108:109], v[104:105]
	v_lshlrev_b32_e32 v106, 16, v207
	v_and_b32_e32 v107, 0xffff0000, v207
	v_rcp_f32_e32 v30, v2
	v_add_f32_e32 v2, 1.0, v31
	v_pk_fma_f32 v[102:103], v[102:103], v[106:107], v[104:105]
	v_rcp_f32_e32 v31, v2
	v_add_f32_e32 v2, 1.0, v24
	v_cvt_pk_bf16_f32 v100, v100, v101
	v_cvt_pk_bf16_f32 v101, v102, v103
	v_lshlrev_b64 v[102:103], 11, v[194:195]
	v_rcp_f32_e32 v24, v2
	v_add_f32_e32 v2, 1.0, v25
	v_mul_f32_e64 v25, v226, -v26
	v_lshl_add_u64 v[102:103], s[14:15], 0, v[102:103]
	v_mul_f32_e32 v25, 0x3fb8aa3b, v25
	v_lshl_add_u64 v[102:103], v[102:103], 0, v[118:119]
	v_exp_f32_e32 v26, v25
	v_mul_f32_e64 v25, v226, -v27
	global_store_dwordx2 v[102:103], v[100:101], off
	v_lshlrev_b32_e32 v100, 16, v192
	v_and_b32_e32 v101, 0xffff0000, v192
	v_mul_f32_e32 v25, 0x3fb8aa3b, v25
	v_mul_f32_e64 v20, v226, -v20
	v_pk_fma_f32 v[96:97], v[96:97], v[100:101], 0 op_sel_hi:[1,1,0]
	v_lshlrev_b32_e32 v100, 16, v190
	v_and_b32_e32 v101, 0xffff0000, v190
	v_exp_f32_e32 v27, v25
	v_mul_f32_e32 v20, 0x3fb8aa3b, v20
	v_mul_f32_e64 v21, v226, -v21
	v_pk_fma_f32 v[92:93], v[92:93], v[100:101], v[96:97]
	v_lshlrev_b32_e32 v96, 16, v188
	v_and_b32_e32 v97, 0xffff0000, v188
	v_exp_f32_e32 v20, v20
	v_mul_f32_e32 v21, 0x3fb8aa3b, v21
	v_pk_fma_f32 v[88:89], v[88:89], v[96:97], v[92:93]
	v_lshlrev_b32_e32 v92, 16, v186
	v_and_b32_e32 v93, 0xffff0000, v186
	v_exp_f32_e32 v21, v21
	v_pk_fma_f32 v[84:85], v[84:85], v[92:93], v[88:89]
	v_lshlrev_b32_e32 v88, 16, v193
	v_and_b32_e32 v89, 0xffff0000, v193
	v_rcp_f32_e32 v25, v2
	v_add_f32_e32 v2, 1.0, v26
	v_pk_fma_f32 v[88:89], v[98:99], v[88:89], 0 op_sel_hi:[1,1,0]
	v_lshlrev_b32_e32 v92, 16, v191
	v_and_b32_e32 v93, 0xffff0000, v191
	v_rcp_f32_e32 v26, v2
	v_add_f32_e32 v2, 1.0, v27
	v_pk_fma_f32 v[88:89], v[94:95], v[92:93], v[88:89]
	v_lshlrev_b32_e32 v92, 16, v189
	v_and_b32_e32 v93, 0xffff0000, v189
	v_rcp_f32_e32 v27, v2
	v_add_f32_e32 v2, 1.0, v20
	v_pk_fma_f32 v[88:89], v[90:91], v[92:93], v[88:89]
	v_lshlrev_b32_e32 v90, 16, v187
	v_and_b32_e32 v91, 0xffff0000, v187
	v_rcp_f32_e32 v20, v2
	v_add_f32_e32 v2, 1.0, v21
	v_pk_fma_f32 v[86:87], v[86:87], v[90:91], v[88:89]
	v_rcp_f32_e32 v21, v2
	v_mul_f32_e64 v2, v226, -v22
	v_cvt_pk_bf16_f32 v84, v84, v85
	v_cvt_pk_bf16_f32 v85, v86, v87
	v_lshlrev_b64 v[86:87], 11, v[184:185]
	v_mul_f32_e32 v2, 0x3fb8aa3b, v2
	v_mul_f32_e64 v22, v226, -v23
	v_lshl_add_u64 v[86:87], s[14:15], 0, v[86:87]
	v_exp_f32_e32 v2, v2
	v_mul_f32_e32 v22, 0x3fb8aa3b, v22
	v_lshl_add_u64 v[86:87], v[86:87], 0, v[118:119]
	v_exp_f32_e32 v23, v22
	global_store_dwordx2 v[86:87], v[84:85], off
	v_lshlrev_b32_e32 v84, 16, v180
	v_and_b32_e32 v85, 0xffff0000, v180
	v_pk_fma_f32 v[80:81], v[80:81], v[84:85], 0 op_sel_hi:[1,1,0]
	v_lshlrev_b32_e32 v84, 16, v178
	v_and_b32_e32 v85, 0xffff0000, v178
	v_pk_fma_f32 v[76:77], v[76:77], v[84:85], v[80:81]
	v_lshlrev_b32_e32 v80, 16, v176
	v_and_b32_e32 v81, 0xffff0000, v176
	v_add_f32_e32 v2, 1.0, v2
	v_pk_fma_f32 v[72:73], v[72:73], v[80:81], v[76:77]
	v_lshlrev_b32_e32 v76, 16, v182
	v_and_b32_e32 v77, 0xffff0000, v182
	v_rcp_f32_e32 v22, v2
	v_add_f32_e32 v2, 1.0, v23
	v_pk_fma_f32 v[68:69], v[68:69], v[76:77], v[72:73]
	v_lshlrev_b32_e32 v72, 16, v181
	v_and_b32_e32 v73, 0xffff0000, v181
	v_rcp_f32_e32 v23, v2
	s_waitcnt vmcnt(7)
	v_mul_f32_e64 v2, v225, -v16
	v_pk_fma_f32 v[72:73], v[82:83], v[72:73], 0 op_sel_hi:[1,1,0]
	v_lshlrev_b32_e32 v76, 16, v179
	v_and_b32_e32 v77, 0xffff0000, v179
	v_mul_f32_e32 v2, 0x3fb8aa3b, v2
	v_mul_f32_e64 v16, v225, -v17
	v_pk_fma_f32 v[72:73], v[78:79], v[76:77], v[72:73]
	v_lshlrev_b32_e32 v76, 16, v177
	v_and_b32_e32 v77, 0xffff0000, v177
	v_exp_f32_e32 v2, v2
	v_mul_f32_e32 v16, 0x3fb8aa3b, v16
	v_pk_fma_f32 v[72:73], v[74:75], v[76:77], v[72:73]
	v_lshlrev_b32_e32 v74, 16, v183
	v_and_b32_e32 v75, 0xffff0000, v183
	v_exp_f32_e32 v17, v16
	v_pk_fma_f32 v[70:71], v[70:71], v[74:75], v[72:73]
	v_cvt_pk_bf16_f32 v68, v68, v69
	v_cvt_pk_bf16_f32 v69, v70, v71
	v_lshlrev_b64 v[70:71], 11, v[174:175]
	v_lshl_add_u64 v[70:71], s[14:15], 0, v[70:71]
	v_add_f32_e32 v2, 1.0, v2
	v_lshl_add_u64 v[70:71], v[70:71], 0, v[118:119]
	v_rcp_f32_e32 v16, v2
	v_add_f32_e32 v2, 1.0, v17
	v_mul_f32_e64 v17, v225, -v18
	global_store_dwordx2 v[70:71], v[68:69], off
	v_lshlrev_b32_e32 v68, 16, v170
	v_and_b32_e32 v69, 0xffff0000, v170
	v_mul_f32_e32 v17, 0x3fb8aa3b, v17
	v_pk_fma_f32 v[64:65], v[64:65], v[68:69], 0 op_sel_hi:[1,1,0]
	v_lshlrev_b32_e32 v68, 16, v168
	v_and_b32_e32 v69, 0xffff0000, v168
	v_exp_f32_e32 v18, v17
	v_mul_f32_e64 v17, v225, -v19
	v_pk_fma_f32 v[60:61], v[60:61], v[68:69], v[64:65]
	v_lshlrev_b32_e32 v64, 16, v166
	v_and_b32_e32 v65, 0xffff0000, v166
	v_mul_f32_e32 v17, 0x3fb8aa3b, v17
	v_mul_f32_e64 v12, v225, -v12
	v_pk_fma_f32 v[56:57], v[56:57], v[64:65], v[60:61]
	v_lshlrev_b32_e32 v60, 16, v172
	v_and_b32_e32 v61, 0xffff0000, v172
	v_exp_f32_e32 v19, v17
	v_mul_f32_e32 v12, 0x3fb8aa3b, v12
	v_mul_f32_e64 v13, v225, -v13
	v_pk_fma_f32 v[52:53], v[52:53], v[60:61], v[56:57]
	v_lshlrev_b32_e32 v56, 16, v171
	v_and_b32_e32 v57, 0xffff0000, v171
	v_exp_f32_e32 v12, v12
	v_mul_f32_e32 v13, 0x3fb8aa3b, v13
	v_pk_fma_f32 v[56:57], v[66:67], v[56:57], 0 op_sel_hi:[1,1,0]
	v_lshlrev_b32_e32 v60, 16, v169
	v_and_b32_e32 v61, 0xffff0000, v169
	v_exp_f32_e32 v13, v13
	v_pk_fma_f32 v[56:57], v[62:63], v[60:61], v[56:57]
	v_lshlrev_b32_e32 v60, 16, v167
	v_and_b32_e32 v61, 0xffff0000, v167
	v_rcp_f32_e32 v17, v2
	v_add_f32_e32 v2, 1.0, v18
	v_pk_fma_f32 v[56:57], v[58:59], v[60:61], v[56:57]
	v_lshlrev_b32_e32 v58, 16, v173
	v_and_b32_e32 v59, 0xffff0000, v173
	v_rcp_f32_e32 v18, v2
	v_add_f32_e32 v2, 1.0, v19
	v_pk_fma_f32 v[54:55], v[54:55], v[58:59], v[56:57]
	v_rcp_f32_e32 v19, v2
	v_add_f32_e32 v2, 1.0, v12
	v_cvt_pk_bf16_f32 v52, v52, v53
	v_cvt_pk_bf16_f32 v53, v54, v55
	v_lshlrev_b64 v[54:55], 11, v[164:165]
	v_rcp_f32_e32 v12, v2
	v_add_f32_e32 v2, 1.0, v13
	v_mul_f32_e64 v13, v225, -v14
	v_lshl_add_u64 v[54:55], s[14:15], 0, v[54:55]
	v_mul_f32_e32 v13, 0x3fb8aa3b, v13
	v_lshl_add_u64 v[54:55], v[54:55], 0, v[118:119]
	v_exp_f32_e32 v14, v13
	v_mul_f32_e64 v13, v225, -v15
	global_store_dwordx2 v[54:55], v[52:53], off
	v_lshlrev_b32_e32 v52, 16, v158
	v_and_b32_e32 v53, 0xffff0000, v158
	v_mul_f32_e32 v13, 0x3fb8aa3b, v13
	v_mul_f32_e64 v8, v225, -v8
	v_pk_fma_f32 v[48:49], v[48:49], v[52:53], 0 op_sel_hi:[1,1,0]
	v_lshlrev_b32_e32 v52, 16, v156
	v_and_b32_e32 v53, 0xffff0000, v156
	v_exp_f32_e32 v15, v13
	v_mul_f32_e32 v8, 0x3fb8aa3b, v8
	v_mul_f32_e64 v9, v225, -v9
	v_pk_fma_f32 v[44:45], v[44:45], v[52:53], v[48:49]
	v_lshlrev_b32_e32 v48, 16, v162
	v_and_b32_e32 v49, 0xffff0000, v162
	v_exp_f32_e32 v8, v8
	v_mul_f32_e32 v9, 0x3fb8aa3b, v9
	v_pk_fma_f32 v[40:41], v[40:41], v[48:49], v[44:45]
	v_lshlrev_b32_e32 v44, 16, v160
	v_and_b32_e32 v45, 0xffff0000, v160
	v_exp_f32_e32 v9, v9
	v_pk_fma_f32 v[36:37], v[36:37], v[44:45], v[40:41]
	v_lshlrev_b32_e32 v40, 16, v159
	v_and_b32_e32 v41, 0xffff0000, v159
	v_rcp_f32_e32 v13, v2
	v_add_f32_e32 v2, 1.0, v14
	v_pk_fma_f32 v[40:41], v[50:51], v[40:41], 0 op_sel_hi:[1,1,0]
	v_lshlrev_b32_e32 v44, 16, v157
	v_and_b32_e32 v45, 0xffff0000, v157
	v_rcp_f32_e32 v14, v2
	v_add_f32_e32 v2, 1.0, v15
	v_pk_fma_f32 v[40:41], v[46:47], v[44:45], v[40:41]
	v_lshlrev_b32_e32 v44, 16, v163
	v_and_b32_e32 v45, 0xffff0000, v163
	v_rcp_f32_e32 v15, v2
	v_add_f32_e32 v2, 1.0, v8
	v_pk_fma_f32 v[40:41], v[42:43], v[44:45], v[40:41]
	v_lshlrev_b32_e32 v42, 16, v161
	v_and_b32_e32 v43, 0xffff0000, v161
	v_rcp_f32_e32 v8, v2
	v_add_f32_e32 v2, 1.0, v9
	v_mul_f32_e64 v9, v225, -v10
	v_pk_fma_f32 v[38:39], v[38:39], v[42:43], v[40:41]
	s_mov_b32 s4, 0x48000
	v_mul_f32_e32 v9, 0x3fb8aa3b, v9
	v_cvt_pk_bf16_f32 v36, v36, v37
	v_cvt_pk_bf16_f32 v37, v38, v39
	v_add_co_u32_e32 v38, vcc, s4, v116
	v_exp_f32_e32 v10, v9
	v_mul_f32_e64 v9, v225, -v11
	v_addc_co_u32_e32 v39, vcc, 0, v117, vcc
	v_mul_f32_e32 v9, 0x3fb8aa3b, v9
	v_mul_f32_e64 v4, v225, -v4
	global_store_dwordx2 v[38:39], v[36:37], off
	v_lshlrev_b32_e32 v36, 16, v148
	v_and_b32_e32 v37, 0xffff0000, v148
	v_exp_f32_e32 v11, v9
	v_mul_f32_e32 v4, 0x3fb8aa3b, v4
	v_mul_f32_e64 v5, v225, -v5
	v_pk_fma_f32 v[32:33], v[32:33], v[36:37], 0 op_sel_hi:[1,1,0]
	v_lshlrev_b32_e32 v36, 16, v154
	v_and_b32_e32 v37, 0xffff0000, v154
	v_exp_f32_e32 v4, v4
	v_mul_f32_e32 v5, 0x3fb8aa3b, v5
	v_pk_fma_f32 v[28:29], v[28:29], v[36:37], v[32:33]
	v_lshlrev_b32_e32 v32, 16, v152
	v_and_b32_e32 v33, 0xffff0000, v152
	v_exp_f32_e32 v5, v5
	v_pk_fma_f32 v[24:25], v[24:25], v[32:33], v[28:29]
	v_lshlrev_b32_e32 v28, 16, v150
	v_and_b32_e32 v29, 0xffff0000, v150
	v_rcp_f32_e32 v9, v2
	v_add_f32_e32 v2, 1.0, v10
	v_pk_fma_f32 v[20:21], v[20:21], v[28:29], v[24:25]
	v_lshlrev_b32_e32 v24, 16, v149
	v_and_b32_e32 v25, 0xffff0000, v149
	v_rcp_f32_e32 v10, v2
	v_add_f32_e32 v2, 1.0, v11
	v_pk_fma_f32 v[24:25], v[34:35], v[24:25], 0 op_sel_hi:[1,1,0]
	v_lshlrev_b32_e32 v28, 16, v155
	v_and_b32_e32 v29, 0xffff0000, v155
	v_rcp_f32_e32 v11, v2
	v_add_f32_e32 v2, 1.0, v4
	v_pk_fma_f32 v[24:25], v[30:31], v[28:29], v[24:25]
	v_lshlrev_b32_e32 v28, 16, v153
	v_and_b32_e32 v29, 0xffff0000, v153
	v_rcp_f32_e32 v4, v2
	v_add_f32_e32 v2, 1.0, v5
	v_pk_fma_f32 v[24:25], v[26:27], v[28:29], v[24:25]
	v_lshlrev_b32_e32 v26, 16, v151
	v_and_b32_e32 v27, 0xffff0000, v151
	v_rcp_f32_e32 v5, v2
	v_mul_f32_e64 v2, v225, -v6
	v_pk_fma_f32 v[22:23], v[22:23], v[26:27], v[24:25]
	s_mov_b32 s4, 0x50000
	v_mul_f32_e32 v2, 0x3fb8aa3b, v2
	v_mul_f32_e64 v6, v225, -v7
	v_cvt_pk_bf16_f32 v20, v20, v21
	v_cvt_pk_bf16_f32 v21, v22, v23
	v_add_co_u32_e32 v22, vcc, s4, v116
	v_exp_f32_e32 v2, v2
	v_mul_f32_e32 v6, 0x3fb8aa3b, v6
	v_addc_co_u32_e32 v23, vcc, 0, v117, vcc
	v_exp_f32_e32 v7, v6
	global_store_dwordx2 v[22:23], v[20:21], off
	s_waitcnt vmcnt(10)
	v_lshlrev_b32_e32 v20, 16, v146
	v_and_b32_e32 v21, 0xffff0000, v146
	v_pk_fma_f32 v[16:17], v[16:17], v[20:21], 0 op_sel_hi:[1,1,0]
	s_waitcnt vmcnt(9)
	v_lshlrev_b32_e32 v20, 16, v144
	v_and_b32_e32 v21, 0xffff0000, v144
	v_pk_fma_f32 v[12:13], v[12:13], v[20:21], v[16:17]
	s_waitcnt vmcnt(8)
	v_lshlrev_b32_e32 v16, 16, v142
	v_and_b32_e32 v17, 0xffff0000, v142
	v_add_f32_e32 v2, 1.0, v2
	v_pk_fma_f32 v[8:9], v[8:9], v[16:17], v[12:13]
	s_waitcnt vmcnt(7)
	v_lshlrev_b32_e32 v12, 16, v140
	v_and_b32_e32 v13, 0xffff0000, v140
	v_rcp_f32_e32 v6, v2
	v_add_f32_e32 v2, 1.0, v7
	v_pk_fma_f32 v[4:5], v[4:5], v[12:13], v[8:9]
	v_rcp_f32_e32 v7, v2
	v_lshlrev_b32_e32 v8, 16, v147
	v_and_b32_e32 v9, 0xffff0000, v147
	v_pk_fma_f32 v[8:9], v[18:19], v[8:9], 0 op_sel_hi:[1,1,0]
	v_lshlrev_b32_e32 v12, 16, v145
	v_and_b32_e32 v13, 0xffff0000, v145
	v_pk_fma_f32 v[8:9], v[14:15], v[12:13], v[8:9]
	v_lshlrev_b32_e32 v12, 16, v143
	v_and_b32_e32 v13, 0xffff0000, v143
	v_pk_fma_f32 v[8:9], v[10:11], v[12:13], v[8:9]
	v_lshlrev_b32_e32 v10, 16, v141
	v_and_b32_e32 v11, 0xffff0000, v141
	v_pk_fma_f32 v[6:7], v[6:7], v[10:11], v[8:9]
	v_cvt_pk_bf16_f32 v4, v4, v5
	v_cvt_pk_bf16_f32 v5, v6, v7
	v_add_co_u32_e32 v6, vcc, 0x58000, v116
	s_mov_b64 s[4:5], -1
	s_nop 0
	v_addc_co_u32_e32 v7, vcc, 0, v117, vcc
	s_andn2_b64 vcc, exec, s[38:39]
	s_mov_b32 s77, 0xc000
	s_mov_b32 s76, 0xe000
	s_movk_i32 s75, 0x3400
	v_readlane_b32 s74, v255, 38
	global_store_dwordx2 v[6:7], v[4:5], off
	s_cbranch_vccnz .LBB0_1036
	s_andn2_b64 vcc, exec, s[10:11]
	s_cbranch_vccnz .LBB0_1035
	s_barrier
	s_branch .LBB0_1035
